# P6 epilogue parameter staging done once per 8-token group (second pass reuses the LDS copy)
# baseline (speedup 1.0000x reference)
.LBB0_975:
	s_add_i32 s0, s96, s35
	s_ashr_i32 s1, s0, 31
	s_lshr_b32 s1, s1, 19
	s_add_i32 s0, s0, s1
	s_ashr_i32 s2, s0, 13
	s_xor_b64 s[14:15], s[6:7], -1
	s_ashr_i32 s0, s2, 31
	s_add_u32 s1, s2, s87
	s_addc_u32 s0, s0, 0
	s_waitcnt vmcnt(0)
	v_lshlrev_b32_e32 v186, 6, v179
	v_lshl_add_u32 v185, v179, 4, s85
	v_mov_b32_e32 v187, 0
	s_bitcmp1_b32 s96, 2
	s_cbranch_scc1 .Lp6_stage_done
	global_load_dwordx4 v[8:11], v186, s[16:17] offset:0
	global_load_dwordx4 v[12:15], v186, s[16:17] offset:16
	global_load_dwordx4 v[16:19], v186, s[16:17] offset:32
	global_load_dwordx4 v[20:23], v186, s[16:17] offset:48
	global_load_dwordx4 v[24:27], v186, s[28:29] offset:0
	global_load_dwordx4 v[28:31], v186, s[28:29] offset:16
	global_load_dwordx4 v[32:35], v186, s[28:29] offset:32
	global_load_dwordx4 v[36:39], v186, s[28:29] offset:48
	global_load_dwordx4 v[40:43], v186, s[12:13] offset:0
	global_load_dwordx4 v[44:47], v186, s[12:13] offset:16
	global_load_dwordx4 v[48:51], v186, s[12:13] offset:32
	global_load_dwordx4 v[52:55], v186, s[12:13] offset:48
	global_load_dwordx4 v[56:59], v186, s[90:91] offset:0
	global_load_dwordx4 v[60:63], v186, s[90:91] offset:16
	global_load_dwordx4 v[64:67], v186, s[90:91] offset:32
	global_load_dwordx4 v[68:71], v186, s[90:91] offset:48
	s_waitcnt vmcnt(0)
	ds_write_b128 v185, v[8:11] offset:0
	ds_write_b128 v185, v[12:15] offset:1024
	ds_write_b128 v185, v[16:19] offset:2048
	ds_write_b128 v185, v[20:23] offset:3072
	ds_write_b128 v185, v[24:27] offset:4096
	ds_write_b128 v185, v[28:31] offset:5120
	ds_write_b128 v185, v[32:35] offset:6144
	ds_write_b128 v185, v[36:39] offset:7168
	ds_write_b128 v185, v[40:43] offset:8192
	ds_write_b128 v185, v[44:47] offset:9216
	ds_write_b128 v185, v[48:51] offset:10240
	ds_write_b128 v185, v[52:55] offset:11264
	ds_write_b128 v185, v[56:59] offset:12288
	ds_write_b128 v185, v[60:63] offset:13312
	ds_write_b128 v185, v[64:67] offset:14336
	ds_write_b128 v185, v[68:71] offset:15360
	s_waitcnt lgkmcnt(0)
.Lp6_stage_done:
	v_readlane_b32 s40, v253, 62
	v_readlane_b32 s41, v253, 63
	s_lshl_b64 s[44:45], s[96:97], 12
	v_lshlrev_b32_e32 v2, 6, v179
	s_add_u32 s40, s40, s44
	s_addc_u32 s41, s41, s45
	s_add_u32 s40, s40, 0x1000
	s_addc_u32 s41, s41, 0
	global_load_dword v4, v2, s[40:41]
	s_add_u32 s40, s40, 0x1000
	s_addc_u32 s41, s41, 0
	global_load_dword v4, v2, s[40:41]
	s_add_u32 s40, s40, 0x1000
	s_addc_u32 s41, s41, 0
	global_load_dword v4, v2, s[40:41]
	v_mov_b32_e32 v1, v179
	s_mulk_i32 s0, 0x6000
	s_mul_hi_u32 s3, s1, 0x6000
	s_add_i32 s3, s3, s0
	s_mulk_i32 s1, 0x6000
	v_lshlrev_b32_e32 v20, 4, v1
	s_add_u32 s6, s70, s1
	v_readlane_b32 s36, v253, 60
	v_ashrrev_i32_e32 v21, 31, v20
	s_addc_u32 s7, s71, s3
	s_lshl_b64 s[0:1], s[96:97], 12
	v_readlane_b32 s38, v253, 62
	v_lshlrev_b64 v[22:23], 2, v[20:21]
	v_readlane_b32 s39, v253, 63
	s_add_u32 s20, s38, s0
	v_lshl_add_u64 v[68:69], s[6:7], 0, v[22:23]
	s_mov_b64 s[6:7], 0x5000
	s_addc_u32 s21, s39, s1
	v_lshl_add_u64 v[12:13], v[68:69], 0, s[6:7]
	s_lshl_b64 s[6:7], s[96:97], 3
	v_lshl_add_u64 v[32:33], s[20:21], 0, v[22:23]
	s_add_u32 s6, s64, s6
	global_load_dwordx4 v[4:7], v[12:13], off offset:48
	global_load_dwordx4 v[8:11], v[12:13], off offset:32
	s_addc_u32 s7, s65, s7
	global_load_dwordx4 v[12:15], v[12:13], off offset:16
	s_nop 0
	global_load_dwordx2 v[72:73], v3, s[6:7]
	global_load_dwordx4 v[16:19], v[32:33], off
	global_load_dwordx4 v[24:27], v[32:33], off offset:16
	global_load_dwordx4 v[28:31], v[32:33], off offset:32
	s_nop 0
	global_load_dwordx4 v[32:35], v[32:33], off offset:48
	v_lshl_add_u64 v[60:61], s[16:17], 0, v[22:23]
	v_lshl_add_u64 v[64:65], s[28:29], 0, v[22:23]
	v_add_co_u32_e32 v68, vcc, s18, v68
	ds_read_b128 v[36:39], v185 offset:7168
	global_load_dword v184, v187, s[28:29]
	ds_read_b128 v[40:43], v185 offset:3072
	global_load_dword v184, v187, s[16:17]
	ds_read_b128 v[44:47], v185 offset:2048
	global_load_dword v184, v187, s[16:17]
	ds_read_b128 v[48:51], v185 offset:6144
	global_load_dword v184, v187, s[28:29]
	ds_read_b128 v[52:55], v185 offset:5120
	global_load_dword v184, v187, s[28:29]
	ds_read_b128 v[56:59], v185 offset:1024
	global_load_dword v184, v187, s[16:17]
	s_nop 0
	ds_read_b128 v[60:63], v185 offset:0
	global_load_dword v184, v187, s[16:17]
	s_nop 0
	ds_read_b128 v[64:67], v185 offset:4096
	global_load_dword v184, v187, s[28:29]
	v_addc_co_u32_e32 v69, vcc, 0, v69, vcc
	global_load_dwordx4 v[68:71], v[68:69], off
	v_add_u32_e32 v142, 64, v183
	v_xor_b32_e32 v1, 1, v178
	v_xor_b32_e32 v2, 2, v178
	v_cmp_lt_i32_e32 vcc, v1, v142
	v_xor_b32_e32 v74, 4, v178
	v_readlane_b32 s20, v255, 42
	v_cndmask_b32_e32 v1, v178, v1, vcc
	v_cmp_lt_i32_e32 vcc, v2, v142
	v_readlane_b32 s22, v255, 44
	s_add_u32 s0, s30, s0
	v_cndmask_b32_e32 v75, v178, v2, vcc
	v_lshlrev_b32_e32 v2, 2, v1
	v_lshlrev_b32_e32 v1, 2, v75
	v_cmp_lt_i32_e32 vcc, v74, v142
	s_addc_u32 s1, s31, s1
	v_readlane_b32 s37, v253, 61
	v_readlane_b32 s40, v254, 0
	v_readlane_b32 s41, v254, 1
	v_readlane_b32 s42, v254, 2
	v_readlane_b32 s43, v254, 3
	v_readlane_b32 s44, v254, 4
	v_readlane_b32 s45, v254, 5
	v_readlane_b32 s46, v254, 6
	v_readlane_b32 s47, v254, 7
	v_readlane_b32 s48, v254, 8
	v_readlane_b32 s49, v254, 9
	v_readlane_b32 s50, v254, 10
	v_readlane_b32 s51, v254, 11
	v_readlane_b32 s21, v255, 43
	v_readlane_b32 s23, v255, 45
	s_waitcnt lgkmcnt(0)
	s_waitcnt vmcnt(14)
	v_pk_add_f32 v[12:13], v[12:13], 1.0 op_sel_hi:[1,0]
	v_pk_add_f32 v[14:15], v[14:15], 1.0 op_sel_hi:[1,0]
	s_waitcnt lgkmcnt(0)
	s_waitcnt vmcnt(12)
	v_pk_add_f32 v[18:19], v[18:19], v[72:73] op_sel_hi:[1,0] neg_lo:[0,1] neg_hi:[0,1]
	v_pk_add_f32 v[4:5], v[4:5], 1.0 op_sel_hi:[1,0]
	v_pk_mul_f32 v[18:19], v[72:73], v[18:19] op_sel:[1,0]
	s_waitcnt lgkmcnt(0)
	s_waitcnt vmcnt(9)
	v_pk_add_f32 v[32:33], v[32:33], v[72:73] op_sel_hi:[1,0] neg_lo:[0,1] neg_hi:[0,1]
	v_pk_add_f32 v[34:35], v[34:35], v[72:73] op_sel_hi:[1,0] neg_lo:[0,1] neg_hi:[0,1]
	v_pk_mul_f32 v[32:33], v[72:73], v[32:33] op_sel:[1,0]
	v_pk_mul_f32 v[34:35], v[72:73], v[34:35] op_sel:[1,0]
	s_waitcnt lgkmcnt(0)
	s_waitcnt vmcnt(7)
	v_pk_fma_f32 v[32:33], v[32:33], v[40:41], v[36:37]
	v_pk_fma_f32 v[34:35], v[34:35], v[42:43], v[38:39]
	v_pk_mul_f32 v[32:33], v[32:33], s[34:35] op_sel_hi:[1,0]
	v_pk_add_f32 v[6:7], v[6:7], 1.0 op_sel_hi:[1,0]
	v_pk_add_f32 v[24:25], v[24:25], v[72:73] op_sel_hi:[1,0] neg_lo:[0,1] neg_hi:[0,1]
	v_pk_mul_f32 v[34:35], v[34:35], s[34:35] op_sel_hi:[1,0]
	v_pk_fma_f32 v[42:43], v[138:139], v[4:5], v[32:33]
	s_waitcnt lgkmcnt(0)
	s_waitcnt vmcnt(1)
	v_pk_fma_f32 v[4:5], v[18:19], v[62:63], v[66:67]
	v_pk_add_f32 v[16:17], v[16:17], v[72:73] op_sel_hi:[1,0] neg_lo:[0,1] neg_hi:[0,1]
	v_pk_mul_f32 v[24:25], v[72:73], v[24:25] op_sel:[1,0]
	v_pk_fma_f32 v[40:41], v[140:141], v[6:7], v[34:35]
	v_pk_mul_f32 v[4:5], v[4:5], s[34:35] op_sel_hi:[1,0]
	s_waitcnt lgkmcnt(0)
	s_waitcnt vmcnt(0)
	v_pk_add_f32 v[6:7], v[70:71], 1.0 op_sel_hi:[1,0]
	v_pk_fma_f32 v[24:25], v[24:25], v[56:57], v[52:53]
	v_pk_fma_f32 v[52:53], v[128:129], v[6:7], v[4:5]
	v_pk_mul_f32 v[4:5], v[72:73], v[16:17] op_sel:[1,0]
	v_pk_add_f32 v[26:27], v[26:27], v[72:73] op_sel_hi:[1,0] neg_lo:[0,1] neg_hi:[0,1]
	v_pk_fma_f32 v[4:5], v[60:61], v[4:5], v[64:65]
	v_pk_mul_f32 v[26:27], v[72:73], v[26:27] op_sel:[1,0]
	v_pk_mul_f32 v[4:5], v[4:5], s[34:35] op_sel_hi:[1,0]
	v_pk_add_f32 v[6:7], v[68:69], 1.0 op_sel_hi:[1,0]
	v_pk_fma_f32 v[26:27], v[26:27], v[58:59], v[54:55]
	v_pk_fma_f32 v[54:55], v[126:127], v[6:7], v[4:5]
	v_pk_add_f32 v[30:31], v[30:31], v[72:73] op_sel_hi:[1,0] neg_lo:[0,1] neg_hi:[0,1]
	v_add_f32_e32 v4, 0, v54
	v_add_f32_e32 v4, v4, v55
	v_pk_mul_f32 v[30:31], v[72:73], v[30:31] op_sel:[1,0]
	v_pk_mul_f32 v[24:25], v[24:25], s[34:35] op_sel_hi:[1,0]
	v_add_f32_e32 v4, v4, v52
	v_pk_add_f32 v[28:29], v[28:29], v[72:73] op_sel_hi:[1,0] neg_lo:[0,1] neg_hi:[0,1]
	v_pk_fma_f32 v[30:31], v[30:31], v[46:47], v[50:51]
	v_pk_fma_f32 v[50:51], v[130:131], v[12:13], v[24:25]
	v_add_f32_e32 v4, v4, v53
	v_pk_mul_f32 v[28:29], v[72:73], v[28:29] op_sel:[1,0]
	v_pk_mul_f32 v[26:27], v[26:27], s[34:35] op_sel_hi:[1,0]
	v_add_f32_e32 v4, v4, v50
	v_pk_fma_f32 v[28:29], v[28:29], v[44:45], v[48:49]
	v_pk_fma_f32 v[48:49], v[132:133], v[14:15], v[26:27]
	v_add_f32_e32 v4, v4, v51
	v_pk_add_f32 v[8:9], v[8:9], 1.0 op_sel_hi:[1,0]
	v_pk_mul_f32 v[28:29], v[28:29], s[34:35] op_sel_hi:[1,0]
	v_add_f32_e32 v4, v4, v48
	v_pk_fma_f32 v[46:47], v[134:135], v[8:9], v[28:29]
	v_add_f32_e32 v4, v4, v49
	v_pk_add_f32 v[10:11], v[10:11], 1.0 op_sel_hi:[1,0]
	v_pk_mul_f32 v[30:31], v[30:31], s[34:35] op_sel_hi:[1,0]
	v_add_f32_e32 v4, v4, v46
	v_pk_fma_f32 v[44:45], v[136:137], v[10:11], v[30:31]
	v_add_f32_e32 v4, v4, v47
	v_add_f32_e32 v4, v4, v44
	v_add_f32_e32 v4, v4, v45
	v_add_f32_e32 v4, v4, v42
	v_add_f32_e32 v4, v4, v43
	v_add_f32_e32 v4, v4, v40
	v_add_f32_e32 v4, v4, v41
	ds_bpermute_b32 v5, v2, v4
	v_cndmask_b32_e32 v6, v178, v74, vcc
	v_lshlrev_b32_e32 v74, 2, v6
	v_xor_b32_e32 v6, 8, v178
	v_cmp_lt_i32_e32 vcc, v6, v142
	s_waitcnt lgkmcnt(0)
	v_add_f32_e32 v4, v4, v5
	ds_bpermute_b32 v5, v1, v4
	v_cndmask_b32_e32 v6, v178, v6, vcc
	v_lshlrev_b32_e32 v75, 2, v6
	v_xor_b32_e32 v6, 16, v178
	v_cmp_lt_i32_e32 vcc, v6, v142
	s_waitcnt lgkmcnt(0)
	v_add_f32_e32 v4, v4, v5
	ds_bpermute_b32 v5, v74, v4
	v_cndmask_b32_e32 v6, v178, v6, vcc
	v_lshlrev_b32_e32 v126, 2, v6
	v_xor_b32_e32 v6, 32, v178
	v_cmp_lt_i32_e32 vcc, v6, v142
	s_waitcnt lgkmcnt(0)
	v_add_f32_e32 v7, v4, v5
	ds_bpermute_b32 v8, v75, v7
	v_cndmask_b32_e32 v4, v178, v6, vcc
	v_lshlrev_b32_e32 v127, 2, v4
	v_lshl_add_u64 v[4:5], s[12:13], 0, v[22:23]
	v_lshl_add_u64 v[36:37], s[90:91], 0, v[22:23]
	s_waitcnt lgkmcnt(0)
	v_add_f32_e32 v24, v7, v8
	ds_bpermute_b32 v25, v126, v24
	ds_read_b128 v[16:19], v185 offset:11264
	global_load_dword v184, v187, s[12:13]
	ds_read_b128 v[12:15], v185 offset:10240
	global_load_dword v184, v187, s[12:13]
	ds_read_b128 v[8:11], v185 offset:9216
	global_load_dword v184, v187, s[12:13]
	s_nop 0
	ds_read_b128 v[4:7], v185 offset:8192
	global_load_dword v184, v187, s[12:13]
	v_lshl_add_u64 v[22:23], s[0:1], 0, v[22:23]
	v_readlane_b32 s0, v255, 23
	v_readlane_b32 s1, v255, 24
	s_waitcnt lgkmcnt(0)
	v_add_f32_e32 v56, v24, v25
	ds_read_b128 v[24:27], v185 offset:15360
	global_load_dword v184, v187, s[90:91]
	ds_read_b128 v[28:31], v185 offset:14336
	global_load_dword v184, v187, s[90:91]
	ds_read_b128 v[32:35], v185 offset:13312
	global_load_dword v184, v187, s[90:91]
	s_nop 0
	ds_read_b128 v[36:39], v185 offset:12288
	global_load_dword v184, v187, s[90:91]
	ds_bpermute_b32 v57, v127, v56
	s_waitcnt lgkmcnt(0)
	v_add_f32_e32 v56, v56, v57
	v_mul_f32_e32 v56, 0x3a800000, v56
	v_pk_add_f32 v[54:55], v[54:55], v[56:57] op_sel_hi:[1,0] neg_lo:[0,1] neg_hi:[0,1]
	v_pk_add_f32 v[52:53], v[52:53], v[56:57] op_sel_hi:[1,0] neg_lo:[0,1] neg_hi:[0,1]
	v_pk_mul_f32 v[58:59], v[54:55], v[54:55]
	v_pk_mul_f32 v[60:61], v[52:53], v[52:53]
	v_add_f32_e32 v58, v58, v59
	v_pk_add_f32 v[50:51], v[50:51], v[56:57] op_sel_hi:[1,0] neg_lo:[0,1] neg_hi:[0,1]
	v_add_f32_e32 v58, v60, v58
	v_pk_mul_f32 v[62:63], v[50:51], v[50:51]
	v_add_f32_e32 v58, v61, v58
	v_pk_add_f32 v[48:49], v[48:49], v[56:57] op_sel_hi:[1,0] neg_lo:[0,1] neg_hi:[0,1]
	v_add_f32_e32 v58, v62, v58
	v_pk_mul_f32 v[64:65], v[48:49], v[48:49]
	v_add_f32_e32 v58, v63, v58
	v_pk_add_f32 v[46:47], v[46:47], v[56:57] op_sel_hi:[1,0] neg_lo:[0,1] neg_hi:[0,1]
	v_add_f32_e32 v58, v64, v58
	v_pk_mul_f32 v[66:67], v[46:47], v[46:47]
	v_add_f32_e32 v58, v65, v58
	v_pk_add_f32 v[44:45], v[44:45], v[56:57] op_sel_hi:[1,0] neg_lo:[0,1] neg_hi:[0,1]
	v_add_f32_e32 v58, v66, v58
	v_pk_mul_f32 v[68:69], v[44:45], v[44:45]
	v_add_f32_e32 v58, v67, v58
	v_pk_add_f32 v[42:43], v[42:43], v[56:57] op_sel_hi:[1,0] neg_lo:[0,1] neg_hi:[0,1]
	v_add_f32_e32 v58, v68, v58
	v_pk_mul_f32 v[70:71], v[42:43], v[42:43]
	v_add_f32_e32 v58, v69, v58
	v_pk_add_f32 v[40:41], v[40:41], v[56:57] op_sel_hi:[1,0] neg_lo:[0,1] neg_hi:[0,1]
	v_add_f32_e32 v58, v70, v58
	v_pk_mul_f32 v[56:57], v[40:41], v[40:41]
	v_add_f32_e32 v58, v71, v58
	v_add_f32_e32 v56, v56, v58
	v_add_f32_e32 v56, v57, v56
	ds_bpermute_b32 v57, v2, v56
	s_waitcnt lgkmcnt(0)
	v_add_f32_e32 v56, v56, v57
	ds_bpermute_b32 v57, v1, v56
	s_waitcnt lgkmcnt(0)
	v_add_f32_e32 v56, v56, v57
	ds_bpermute_b32 v57, v74, v56
	s_waitcnt lgkmcnt(0)
	v_add_f32_e32 v56, v56, v57
	ds_bpermute_b32 v57, v75, v56
	s_waitcnt lgkmcnt(0)
	v_add_f32_e32 v56, v56, v57
	ds_bpermute_b32 v57, v126, v56
	s_waitcnt lgkmcnt(0)
	v_add_f32_e32 v56, v56, v57
	ds_bpermute_b32 v57, v127, v56
	s_waitcnt lgkmcnt(0)
	v_add_f32_e32 v56, v56, v57
	v_fmamk_f32 v56, v56, 0x3a800000, v204
	v_mul_f32_e32 v57, 0x4b800000, v56
	v_cmp_gt_f32_e32 vcc, s22, v56
	s_nop 1
	v_cndmask_b32_e32 v56, v56, v57, vcc
	v_rsq_f32_e32 v56, v56
	s_nop 0
	v_mul_f32_e32 v57, 0x45800000, v56
	v_cndmask_b32_e32 v56, v56, v57, vcc
	v_pk_mul_f32 v[54:55], v[54:55], v[56:57] op_sel_hi:[1,0]
	v_pk_mul_f32 v[52:53], v[52:53], v[56:57] op_sel_hi:[1,0]
	s_waitcnt lgkmcnt(0)
	s_waitcnt vmcnt(0)
	v_pk_fma_f32 v[4:5], v[4:5], v[54:55], v[36:37]
	v_pk_mul_f32 v[36:37], v[50:51], v[56:57] op_sel_hi:[1,0]
	v_pk_fma_f32 v[6:7], v[6:7], v[52:53], v[38:39]
	v_pk_fma_f32 v[8:9], v[8:9], v[36:37], v[32:33]
	v_pk_mul_f32 v[32:33], v[48:49], v[56:57] op_sel_hi:[1,0]
	s_and_b64 vcc, exec, s[0:1]
	v_pk_fma_f32 v[10:11], v[10:11], v[32:33], v[34:35]
	v_pk_mul_f32 v[32:33], v[46:47], v[56:57] op_sel_hi:[1,0]
	s_nop 0
	v_pk_fma_f32 v[12:13], v[12:13], v[32:33], v[28:29]
	v_pk_mul_f32 v[28:29], v[44:45], v[56:57] op_sel_hi:[1,0]
	s_nop 0
	v_pk_fma_f32 v[14:15], v[14:15], v[28:29], v[30:31]
	v_pk_mul_f32 v[28:29], v[42:43], v[56:57] op_sel_hi:[1,0]
	s_nop 0
	v_pk_fma_f32 v[16:17], v[16:17], v[28:29], v[24:25]
	v_pk_mul_f32 v[24:25], v[40:41], v[56:57] op_sel_hi:[1,0]
	s_nop 0
	v_pk_fma_f32 v[18:19], v[18:19], v[24:25], v[26:27]
	global_store_dwordx4 v[22:23], v[4:7], off
	global_store_dwordx4 v[22:23], v[8:11], off offset:16
	global_store_dwordx4 v[22:23], v[12:15], off offset:32
	global_store_dwordx4 v[22:23], v[16:19], off offset:48
	s_cbranch_vccz .LBB0_977
	s_lshl_b64 s[0:1], s[96:97], 10
	s_mul_hi_i32 s3, s2, 0x6000
	s_mulk_i32 s2, 0x6000
	s_add_u32 s2, s70, s2
	s_addc_u32 s3, s71, s3
	v_lshl_add_u64 v[50:51], v[20:21], 2, s[2:3]
	s_mov_b64 s[2:3], 0x19000
	v_add_co_u32_e32 v34, vcc, s86, v50
	v_lshl_add_u64 v[30:31], v[50:51], 0, s[2:3]
	s_mov_b64 s[2:3], 0x18000
	v_addc_co_u32_e32 v35, vcc, 0, v51, vcc
	v_lshl_add_u64 v[46:47], v[50:51], 0, s[2:3]
	v_add_co_u32_e32 v50, vcc, s67, v50
	global_load_dwordx4 v[22:25], v[30:31], off offset:32
	global_load_dwordx4 v[26:29], v[30:31], off offset:16
	v_addc_co_u32_e32 v51, vcc, 0, v51, vcc
	global_load_dwordx4 v[30:33], v[30:31], off offset:48
	s_nop 0
	global_load_dwordx4 v[34:37], v[34:35], off
	s_nop 0
	global_load_dwordx4 v[38:41], v[46:47], off offset:16
	global_load_dwordx4 v[42:45], v[46:47], off offset:48
	s_nop 0
	global_load_dwordx4 v[46:49], v[46:47], off offset:32
	s_lshl_b64 s[0:1], s[0:1], 1
	global_load_dwordx4 v[50:53], v[50:51], off
	s_add_u32 s0, s76, s0
	s_addc_u32 s1, s77, s1
	v_lshl_add_u64 v[20:21], v[20:21], 1, s[0:1]
	s_waitcnt lgkmcnt(0)
	s_waitcnt vmcnt(7)
	v_pk_add_f32 v[22:23], v[22:23], 1.0 op_sel_hi:[1,0]
	s_waitcnt lgkmcnt(0)
	s_waitcnt vmcnt(6)
	v_pk_add_f32 v[26:27], v[26:27], 1.0 op_sel_hi:[1,0]
	v_pk_add_f32 v[28:29], v[28:29], 1.0 op_sel_hi:[1,0]
	s_waitcnt lgkmcnt(0)
	s_waitcnt vmcnt(4)
	v_pk_add_f32 v[34:35], v[34:35], 1.0 op_sel_hi:[1,0]
	v_pk_add_f32 v[36:37], v[36:37], 1.0 op_sel_hi:[1,0]
	v_pk_add_f32 v[24:25], v[24:25], 1.0 op_sel_hi:[1,0]
	v_pk_add_f32 v[30:31], v[30:31], 1.0 op_sel_hi:[1,0]
	v_pk_add_f32 v[32:33], v[32:33], 1.0 op_sel_hi:[1,0]
	s_waitcnt lgkmcnt(0)
	s_waitcnt vmcnt(3)
	v_pk_fma_f32 v[8:9], v[8:9], v[26:27], v[38:39]
	v_pk_fma_f32 v[10:11], v[10:11], v[28:29], v[40:41]
	s_waitcnt lgkmcnt(0)
	s_waitcnt vmcnt(1)
	v_pk_fma_f32 v[12:13], v[12:13], v[22:23], v[46:47]
	s_waitcnt lgkmcnt(0)
	s_waitcnt vmcnt(0)
	v_pk_fma_f32 v[4:5], v[4:5], v[34:35], v[50:51]
	v_pk_fma_f32 v[22:23], v[6:7], v[36:37], v[52:53]
	v_pk_fma_f32 v[14:15], v[14:15], v[24:25], v[48:49]
	v_pk_fma_f32 v[16:17], v[16:17], v[30:31], v[42:43]
	v_pk_fma_f32 v[18:19], v[18:19], v[32:33], v[44:45]
	v_cvt_pk_bf16_f32 v6, v8, v9
	v_cvt_pk_bf16_f32 v7, v10, v11
	v_cvt_pk_bf16_f32 v4, v4, v5
	v_cvt_pk_bf16_f32 v5, v22, v23
	v_cvt_pk_bf16_f32 v8, v12, v13
	v_cvt_pk_bf16_f32 v9, v14, v15
	v_cvt_pk_bf16_f32 v10, v16, v17
	v_cvt_pk_bf16_f32 v11, v18, v19
	global_store_dwordx4 v[20:21], v[4:7], off
	global_store_dwordx4 v[20:21], v[8:11], off offset:16
